# speedup vs baseline: 1.2767x; 1.0197x over previous
.Lpoll_issued:
	s_waitcnt lgkmcnt(0)
	v_mfma_f32_16x16x32_f16 v[6:9], v[130:133], v[180:183], v[6:9]
	s_add_i32 s12, s24, -1
	s_bfe_i32 s13, s12, 0x10001
	s_and_b32 s30, s13, 0x40004000
	v_mfma_f32_16x16x32_f16 v[10:13], v[126:129], v[180:183], v[10:13]
	v_mov_b32_e32 v3, 0xbfffbfff
	v_cndmask_b32_e64 v167, 0, v3, s[2:3]
	s_lshl_b32 s34, s24, 13
	v_mfma_f32_16x16x32_f16 v[14:17], v[122:125], v[180:183], v[14:17]
	s_and_b32 s34, s34, 0x4000
	s_lshl_b32 s14, s24, 10
	v_lshl_add_u64 v[178:179], s[14:15], 2, v[96:97]
	v_mfma_f32_16x16x32_f16 v[18:21], v[118:121], v[180:183], v[18:21]
	v_bitop3_b32 v2, s27, v193, 1 bitop3:0x6c
	v_add_u32_e32 v2, s27, v2
	v_min_i32_e32 v2, 0x1ff, v2
	v_mfma_f32_16x16x32_f16 v[22:25], v[114:117], v[180:183], v[22:25]
	s_and_b32 s12, s27, 1
	v_lshlrev_b32_e32 v200, 11, v2
	v_lshl_add_u64 v[2:3], v[210:211], 0, v[200:201]
	v_mfma_f32_16x16x32_f16 v[26:29], v[110:113], v[180:183], v[26:29]
	s_lshl_b32 s14, s12, 8
	v_lshl_add_u64 v[4:5], v[2:3], 0, s[14:15]
	s_lshl_b32 s35, s16, 14
	v_mfma_f32_16x16x32_f16 v[30:33], v[194:197], v[180:183], v[30:33]
	s_bitset1_b32 s35, 17
	s_add_i32 s26, s35, s21
	v_lshlrev_b32_e32 v2, 4, v217
	v_mfma_f32_16x16x32_f16 v[34:37], v[202:205], v[180:183], v[34:37]
	v_add3_u32 v174, s26, v2, v103
	s_lshl_b32 s12, s20, 4
	s_add_i32 s12, s12, s35
	s_waitcnt lgkmcnt(0)
	v_mfma_f32_16x16x32_f16 v[6:9], v[162:165], v[218:221], v[6:9]
	v_add3_u32 v175, s12, v105, v103
	v_lshl_add_u32 v176, s16, 17, v106
	v_mfma_f32_16x16x32_f16 v[10:13], v[158:161], v[218:221], v[10:13]
	s_and_b32 s31, s24, 15
	s_and_b32 s12, s24, 0x1f0
	v_mfma_f32_16x16x32_f16 v[14:17], v[154:157], v[218:221], v[14:17]
	s_add_i32 s12, s23, s12
	s_min_i32 s12, s12, 0x1ff
	v_mfma_f32_16x16x32_f16 v[18:21], v[150:153], v[218:221], v[18:21]
	s_ashr_i32 s13, s12, 31
	s_lshl_b64 s[12:13], s[12:13], 11
	v_mfma_f32_16x16x32_f16 v[22:25], v[146:149], v[218:221], v[22:25]
	v_lshl_add_u64 v[172:173], v[0:1], 0, s[12:13]
	v_mfma_f32_16x16x32_f16 v[26:29], v[142:145], v[218:221], v[26:29]
	v_mfma_f32_16x16x32_f16 v[30:33], v[138:141], v[218:221], v[30:33]
	v_mfma_f32_16x16x32_f16 v[34:37], v[134:137], v[218:221], v[34:37]
	s_cmp_eq_u32 s24, 0
	s_cbranch_scc1 .Lfirst_step
	s_waitcnt vmcnt(7)
	v_bitop3_b32 v168, v62, v63, s30 bitop3:0x7e
	v_bitop3_b32 v169, v64, v65, s30 bitop3:0x7e
	v_bitop3_b32 v168, v168, v169, s18 bitop3:0xa8
	v_cmp_ne_u32_e32 vcc, 0, v168
	s_cbranch_vccnz .Lrestart0
	v_and_b32_e32 v62, v62, v167
	v_and_b32_e32 v63, v63, v167
	v_and_b32_e32 v64, v64, v167
	v_and_b32_e32 v65, v65, v167
	s_nop 1

.Lfast7:
	v_mfma_f32_16x16x32_f16 v[6:9], a[28:31], v[90:93], v[6:9]
	global_load_dwordx4 v[46:49], v[4:5], off
	v_mfma_f32_16x16x32_f16 v[10:13], a[60:63], v[90:93], v[10:13]
	global_load_dwordx4 v[50:53], v[4:5], off offset:16
	v_mfma_f32_16x16x32_f16 v[14:17], a[92:95], v[90:93], v[14:17]
	global_load_dwordx4 v[38:41], v[4:5], off offset:128
	v_mfma_f32_16x16x32_f16 v[18:21], a[124:127], v[90:93], v[18:21]
	global_load_dwordx4 v[42:45], v[4:5], off offset:144
	v_mfma_f32_16x16x32_f16 v[22:25], a[156:159], v[90:93], v[22:25]
	s_cmp_lg_u32 s31, 0
	s_cbranch_scc1 .Lno_warm
	global_load_dwordx4 v[54:57], v[172:173], off
	global_load_dwordx4 v[58:61], v[172:173], off offset:1024
.Lno_warm:
	v_mfma_f32_16x16x32_f16 v[26:29], a[188:191], v[90:93], v[26:29]
	v_mfma_f32_16x16x32_f16 v[30:33], a[220:223], v[90:93], v[30:33]
	v_mfma_f32_16x16x32_f16 v[34:37], a[252:255], v[90:93], v[34:37]
.Lall_chunks_done:
	s_and_saveexec_b64 s[12:13], s[2:3]
	ds_write_b128 v174, v[6:9]
	ds_write_b128 v174, v[10:13] offset:512
	ds_write_b128 v174, v[14:17] offset:1024
	ds_write_b128 v174, v[18:21] offset:1536
	ds_write_b128 v174, v[22:25] offset:2048
	ds_write_b128 v174, v[26:29] offset:2560
	ds_write_b128 v174, v[30:33] offset:3072
	ds_write_b128 v174, v[34:37] offset:3584
	s_or_b64 exec, exec, s[12:13]
	s_waitcnt lgkmcnt(0)
	s_barrier
	ds_read_b128 v[2:5], v175
	ds_read_b128 v[224:227], v175 offset:4096
	ds_read_b128 v[228:231], v175 offset:8192
	ds_read_b128 v[232:235], v175 offset:12288
	s_mov_b64 exec, s[2:3]
	v_mov_b64_e32 v[6:7], 0
	v_mov_b64_e32 v[8:9], 0
	v_mov_b64_e32 v[10:11], 0
	v_mov_b64_e32 v[12:13], 0
	v_mov_b64_e32 v[14:15], 0
	v_mov_b64_e32 v[16:17], 0
	v_mov_b64_e32 v[18:19], 0
	v_mov_b64_e32 v[20:21], 0
	v_mov_b64_e32 v[22:23], 0
	v_mov_b64_e32 v[24:25], 0
	v_mov_b64_e32 v[26:27], 0
	v_mov_b64_e32 v[28:29], 0
	v_mov_b64_e32 v[30:31], 0
	v_mov_b64_e32 v[32:33], 0
	v_mov_b64_e32 v[34:35], 0
	v_mov_b64_e32 v[36:37], 0
	s_mov_b64 exec, -1
	s_waitcnt lgkmcnt(0)
	v_pk_add_f32 v[4:5], v[4:5], v[226:227]
	v_pk_add_f32 v[2:3], v[2:3], v[224:225]
	v_pk_add_f32 v[4:5], v[4:5], v[230:231]
	v_pk_add_f32 v[2:3], v[2:3], v[228:229]
	v_pk_add_f32 v[4:5], v[4:5], v[234:235]
	v_pk_add_f32 v[2:3], v[2:3], v[232:233]
	v_fma_f32 v4, v4, s37, v187
	v_fma_f32 v2, v2, s38, v185
	v_exp_f32_e32 v4, v4
	v_fma_f32 v3, v3, s38, v186
	v_exp_f32_e32 v2, v2
	v_fma_f32 v5, v5, s38, v188
	v_exp_f32_e32 v3, v3
	v_add_f32_e32 v4, 1.0, v4
	v_add_f32_e32 v2, 1.0, v2
	v_rcp_f32_e32 v4, v4
	v_rcp_f32_e32 v2, v2
	v_add_f32_e32 v3, 1.0, v3
	v_rcp_f32_e32 v3, v3
	v_exp_f32_e32 v5, v5
	v_fma_f32 v4, v4, -2.0, 1.0
	v_mul_f32_e32 v2, v2, v4
	v_add_f32_e32 v4, 1.0, v5
	v_fmac_f32_e32 v2, v177, v3
	v_rcp_f32_e32 v5, v4
	v_mul_f32_e32 v3, 0x4038aa3b, v2
	v_exp_f32_e32 v3, v3
	v_mov_b32_e32 v177, v2
	v_add_f32_e32 v3, 1.0, v3
	v_rcp_f32_e32 v3, v3
	s_nop 0
	v_fma_f32 v3, v3, -2.0, 1.0
	v_mul_f32_e32 v4, v5, v3
	v_fma_mixlo_f16 v3, v5, v3, 0
	v_and_b32_e32 v3, 0xffffbfff, v3
	v_or_b32_sdwa v108, s34, v3 dst_sel:DWORD dst_unused:UNUSED_PAD src0_sel:DWORD src1_sel:WORD_0
	s_nop 1
	v_mov_b32_dpp v109, v108 row_ror:8 row_mask:0xf bank_mask:0xf
	v_mov_b32_dpp v5, v4 row_ror:8 row_mask:0xf bank_mask:0xf
	s_and_saveexec_b64 s[12:13], s[0:1]
	v_lshl_or_b32 v108, v109, 16, v108
	s_andn2_b64 vcc, exec, s[4:5]
	s_cbranch_vccnz .Lpub_sc1
	buffer_store_dword v108, v176, s[8:11], 0 offen

.Lfirst_step:
	s_waitcnt vmcnt(0)
	v_cvt_pk_f16_f32 v180, v46, v47
	v_cvt_pk_f16_f32 v181, v48, v49
	v_cvt_pk_f16_f32 v182, v50, v51
	v_cvt_pk_f16_f32 v183, v52, v53
	v_cvt_pk_f16_f32 v218, v38, v39
	v_cvt_pk_f16_f32 v219, v40, v41
	v_cvt_pk_f16_f32 v220, v42, v43
	v_cvt_pk_f16_f32 v221, v44, v45
	v_xor_b32_e32 v222, 0x4000, v222
	ds_read_b128 v[130:133], v222
	ds_read_b128 v[126:129], v222 offset:1024
	ds_read_b128 v[122:125], v222 offset:2048
	ds_read_b128 v[118:121], v222 offset:3072
	ds_read_b128 v[114:117], v222 offset:4096
	ds_read_b128 v[110:113], v222 offset:5120
	ds_read_b128 v[194:197], v222 offset:6144
	ds_read_b128 v[202:205], v222 offset:7168
	ds_read_b128 v[162:165], v222 offset:8192
	ds_read_b128 v[158:161], v222 offset:9216
	ds_read_b128 v[154:157], v222 offset:10240
	ds_read_b128 v[150:153], v222 offset:11264
	ds_read_b128 v[146:149], v222 offset:12288
	ds_read_b128 v[142:145], v222 offset:13312
	ds_read_b128 v[138:141], v222 offset:14336
	ds_read_b128 v[134:137], v222 offset:15360
	global_load_dwordx4 v[46:49], v[4:5], off
	global_load_dwordx4 v[50:53], v[4:5], off offset:16
	global_load_dwordx4 v[38:41], v[4:5], off offset:128
	global_load_dwordx4 v[42:45], v[4:5], off offset:144
	global_load_dwordx4 v[54:57], v[172:173], off
	global_load_dwordx4 v[58:61], v[172:173], off offset:1024
	s_branch .Lall_chunks_done
